# speedup vs baseline: 1.0476x; 1.0026x over previous
.Lca_ok_1:
	buffer_load_dwordx4 v[42:45], v117, s[4:7], 0 offen offset:0 sc1
	ds_read_b128 v[50:53], v116 offset:256
	s_setprio 0
	v_exp_f32_e32 v94, v86
	v_exp_f32_e32 v95, v90
	v_exp_f32_e32 v96, v84
	v_exp_f32_e32 v97, v88
	v_exp_f32_e32 v98, v85
	v_exp_f32_e32 v99, v89
	v_pk_add_f32 v[100:101], v[94:95], 1.0 op_sel_hi:[1,0]
	v_pk_fma_f32 v[102:103], v[94:95], s[8:9], v[92:93] op_sel_hi:[1,0,0]
	v_pk_fma_f32 v[100:101], v[96:97], v[100:101], v[100:101]
	v_pk_fma_f32 v[104:105], v[100:101], v[98:99], v[100:101]
	v_rcp_f32_e32 v104, v104
	v_rcp_f32_e32 v105, v105
	v_pk_fma_f32 v[102:103], v[102:103], v[98:99], v[102:103]
	v_pk_fma_f32 v[102:103], v[64:65], v[100:101], v[102:103]
	v_exp_f32_e32 v106, v87
	v_pk_mul_f32 v[64:65], v[102:103], v[104:105]
	v_exp_f32_e32 v108, v64
	v_exp_f32_e32 v109, v65
	v_exp_f32_e32 v107, v91
	v_pk_add_f32 v[110:111], v[108:109], 1.0 op_sel_hi:[1,0]
	v_pk_fma_f32 v[110:111], v[110:111], v[106:107], v[110:111]
	v_rcp_f32_e32 v110, v110
	v_rcp_f32_e32 v111, v111
	v_pk_add_f32 v[112:113], v[108:109], -1.0 op_sel_hi:[1,0]
	v_pk_mul_f32 v[112:113], v[112:113], v[110:111]
	v_cvt_pk_f16_f32 v114, v112, v113
	ds_write_b32 v81, v114 offset:0
	s_waitcnt lgkmcnt(0)
	s_setprio 2
	s_barrier
	v_mfma_f32_16x16x32_f16 v[84:87], v[6:9], v[50:53], v[18:21]
	v_mfma_f32_16x16x32_f16 v[88:91], v[10:13], v[50:53], v[38:41]
	ds_read_b128 v[56:59], v75 offset:0
	ds_read_b128 v[60:63], v75 offset:1024
	s_waitcnt vmcnt(3)
	v_mfma_f32_16x16x32_f16 v[84:87], v[2:5], v[46:49], v[84:87]
	v_mfma_f32_16x16x32_f16 v[88:91], v[14:17], v[46:49], v[88:91]
	s_waitcnt lgkmcnt(1)
	v_mfma_f32_16x16x32_f16 v[84:87], v[30:33], v[56:59], v[84:87]
	v_mfma_f32_16x16x32_f16 v[88:91], v[22:25], v[56:59], v[88:91]
	s_waitcnt lgkmcnt(0)
	v_mfma_f32_16x16x32_f16 v[84:87], v[34:37], v[60:63], v[84:87]
	v_mfma_f32_16x16x32_f16 v[88:91], v[26:29], v[60:63], v[88:91]
	s_add_u32 s13, s12, 4
	s_min_u32 s13, s13, 450
	s_cmp_ge_u32 s14, s13
	s_cbranch_scc0 .Lca_slow_6

.Lca_loop:
	s_setprio 2
	s_barrier
	v_mfma_f32_16x16x32_f16 v[84:87], v[6:9], v[50:53], v[18:21]
	v_mfma_f32_16x16x32_f16 v[88:91], v[10:13], v[50:53], v[38:41]
	ds_read_b128 v[56:59], v75 offset:2048
	ds_read_b128 v[60:63], v75 offset:3072
	s_waitcnt vmcnt(1)
	v_mfma_f32_16x16x32_f16 v[84:87], v[2:5], v[42:45], v[84:87]
	v_mfma_f32_16x16x32_f16 v[88:91], v[14:17], v[42:45], v[88:91]
	v_readfirstlane_b32 s10, v67
	v_readfirstlane_b32 s11, v68
	global_load_dword v67, v66, s[0:1] sc1
	global_load_dword v68, v66, s[0:1] offset:4 sc1
	s_min_u32 s10, s10, s11
	s_max_u32 s14, s14, s10
	s_waitcnt lgkmcnt(1)
	v_mfma_f32_16x16x32_f16 v[84:87], v[30:33], v[56:59], v[84:87]
	v_mfma_f32_16x16x32_f16 v[88:91], v[22:25], v[56:59], v[88:91]
	s_waitcnt lgkmcnt(0)
	v_mfma_f32_16x16x32_f16 v[84:87], v[34:37], v[60:63], v[84:87]
	v_mfma_f32_16x16x32_f16 v[88:91], v[26:29], v[60:63], v[88:91]
	s_add_u32 s13, s12, 3
	s_min_u32 s13, s13, 450
	s_cmp_ge_u32 s14, s13
	s_cbranch_scc0 .Lca_slow_9
.Lca_ok_7:
	buffer_load_dwordx4 v[42:45], v117, s[4:7], 0 offen offset:0 sc1
	ds_read_b128 v[50:53], v116 offset:256
	s_setprio 0
	v_min_f32_e32 v64, 0x42700000, v64
	v_min_f32_e32 v65, 0x42700000, v65
	v_exp_f32_e32 v94, v86
	v_exp_f32_e32 v95, v90
	v_exp_f32_e32 v96, v84
	v_exp_f32_e32 v97, v88
	v_exp_f32_e32 v98, v85
	v_exp_f32_e32 v99, v89
	v_pk_add_f32 v[100:101], v[94:95], 1.0 op_sel_hi:[1,0]
	v_pk_fma_f32 v[102:103], v[94:95], s[8:9], v[92:93] op_sel_hi:[1,0,0]
	v_pk_fma_f32 v[100:101], v[96:97], v[100:101], v[100:101]
	v_pk_fma_f32 v[104:105], v[100:101], v[98:99], v[100:101]
	v_rcp_f32_e32 v104, v104
	v_rcp_f32_e32 v105, v105
	v_pk_fma_f32 v[102:103], v[102:103], v[98:99], v[102:103]
	v_pk_fma_f32 v[102:103], v[64:65], v[100:101], v[102:103]
	v_exp_f32_e32 v106, v87
	v_pk_mul_f32 v[64:65], v[102:103], v[104:105]
	v_exp_f32_e32 v108, v64
	v_exp_f32_e32 v109, v65
	v_exp_f32_e32 v107, v91
	v_pk_add_f32 v[110:111], v[108:109], 1.0 op_sel_hi:[1,0]
	v_pk_fma_f32 v[110:111], v[110:111], v[106:107], v[110:111]
	v_rcp_f32_e32 v110, v110
	v_rcp_f32_e32 v111, v111
	v_pk_add_f32 v[112:113], v[108:109], -1.0 op_sel_hi:[1,0]
	v_pk_mul_f32 v[112:113], v[112:113], v[110:111]
	v_cvt_pk_f16_f32 v114, v112, v113
	ds_write_b32 v81, v114 offset:0
	s_waitcnt lgkmcnt(0)
	s_setprio 2
	s_barrier
	v_mfma_f32_16x16x32_f16 v[84:87], v[6:9], v[50:53], v[18:21]
	v_mfma_f32_16x16x32_f16 v[88:91], v[10:13], v[50:53], v[38:41]
	ds_read_b128 v[56:59], v75 offset:0
	ds_read_b128 v[60:63], v75 offset:1024
	s_waitcnt vmcnt(3)
	v_mfma_f32_16x16x32_f16 v[84:87], v[2:5], v[46:49], v[84:87]
	v_mfma_f32_16x16x32_f16 v[88:91], v[14:17], v[46:49], v[88:91]
	s_waitcnt lgkmcnt(1)
	v_mfma_f32_16x16x32_f16 v[84:87], v[30:33], v[56:59], v[84:87]
	v_mfma_f32_16x16x32_f16 v[88:91], v[22:25], v[56:59], v[88:91]
	s_waitcnt lgkmcnt(0)
	v_mfma_f32_16x16x32_f16 v[84:87], v[34:37], v[60:63], v[84:87]
	v_mfma_f32_16x16x32_f16 v[88:91], v[26:29], v[60:63], v[88:91]
	s_add_u32 s13, s12, 4
	s_min_u32 s13, s13, 450
	s_cmp_ge_u32 s14, s13
	s_cbranch_scc0 .Lca_slow_12
.Lca_ok_10:
	buffer_load_dwordx4 v[46:49], v117, s[4:7], 0 offen offset:1024 sc1
	ds_read_b128 v[50:53], v116 offset:512
	s_setprio 0
	v_exp_f32_e32 v94, v86
	v_exp_f32_e32 v95, v90
	v_exp_f32_e32 v96, v84
	v_exp_f32_e32 v97, v88
	v_exp_f32_e32 v98, v85
	v_exp_f32_e32 v99, v89
	v_pk_add_f32 v[100:101], v[94:95], 1.0 op_sel_hi:[1,0]
	v_pk_fma_f32 v[102:103], v[94:95], s[8:9], v[92:93] op_sel_hi:[1,0,0]
	v_pk_fma_f32 v[100:101], v[96:97], v[100:101], v[100:101]
	v_pk_fma_f32 v[104:105], v[100:101], v[98:99], v[100:101]
	v_rcp_f32_e32 v104, v104
	v_rcp_f32_e32 v105, v105
	v_pk_fma_f32 v[102:103], v[102:103], v[98:99], v[102:103]
	v_pk_fma_f32 v[102:103], v[64:65], v[100:101], v[102:103]
	v_exp_f32_e32 v106, v87
	v_pk_mul_f32 v[64:65], v[102:103], v[104:105]
	v_exp_f32_e32 v108, v64
	v_exp_f32_e32 v109, v65
	v_exp_f32_e32 v107, v91
	v_pk_add_f32 v[110:111], v[108:109], 1.0 op_sel_hi:[1,0]
	v_pk_fma_f32 v[110:111], v[110:111], v[106:107], v[110:111]
	v_rcp_f32_e32 v110, v110
	v_rcp_f32_e32 v111, v111
	v_pk_add_f32 v[112:113], v[108:109], -1.0 op_sel_hi:[1,0]
	v_pk_mul_f32 v[112:113], v[112:113], v[110:111]
	v_cvt_pk_f16_f32 v114, v112, v113
	ds_write_b32 v81, v114 offset:2048
	s_waitcnt lgkmcnt(0)
	s_setprio 2
	s_barrier
	v_mfma_f32_16x16x32_f16 v[84:87], v[6:9], v[50:53], v[18:21]
	v_mfma_f32_16x16x32_f16 v[88:91], v[10:13], v[50:53], v[38:41]
	ds_read_b128 v[56:59], v75 offset:2048
	ds_read_b128 v[60:63], v75 offset:3072
	s_waitcnt vmcnt(1)
	v_mfma_f32_16x16x32_f16 v[84:87], v[2:5], v[42:45], v[84:87]
	v_mfma_f32_16x16x32_f16 v[88:91], v[14:17], v[42:45], v[88:91]
	v_readfirstlane_b32 s10, v67
	v_readfirstlane_b32 s11, v68
	global_load_dword v67, v66, s[0:1] sc1
	global_load_dword v68, v66, s[0:1] offset:4 sc1
	s_min_u32 s10, s10, s11
	s_max_u32 s14, s14, s10
	s_waitcnt lgkmcnt(1)
	v_mfma_f32_16x16x32_f16 v[84:87], v[30:33], v[56:59], v[84:87]
	v_mfma_f32_16x16x32_f16 v[88:91], v[22:25], v[56:59], v[88:91]
	s_waitcnt lgkmcnt(0)
	v_mfma_f32_16x16x32_f16 v[84:87], v[34:37], v[60:63], v[84:87]
	v_mfma_f32_16x16x32_f16 v[88:91], v[26:29], v[60:63], v[88:91]
	s_add_u32 s13, s12, 5
	s_min_u32 s13, s13, 450
	s_cmp_ge_u32 s14, s13
	s_cbranch_scc0 .Lca_slow_15
.Lca_ok_13:
	buffer_load_dwordx4 v[42:45], v117, s[4:7], 0 offen offset:2048 sc1
	ds_read_b128 v[50:53], v116 offset:768
	s_setprio 0
	v_exp_f32_e32 v94, v86
	v_exp_f32_e32 v95, v90
	v_exp_f32_e32 v96, v84
	v_exp_f32_e32 v97, v88
	v_exp_f32_e32 v98, v85
	v_exp_f32_e32 v99, v89
	v_pk_add_f32 v[100:101], v[94:95], 1.0 op_sel_hi:[1,0]
	v_pk_fma_f32 v[102:103], v[94:95], s[8:9], v[92:93] op_sel_hi:[1,0,0]
	v_pk_fma_f32 v[100:101], v[96:97], v[100:101], v[100:101]
	v_pk_fma_f32 v[104:105], v[100:101], v[98:99], v[100:101]
	v_rcp_f32_e32 v104, v104
	v_rcp_f32_e32 v105, v105
	v_pk_fma_f32 v[102:103], v[102:103], v[98:99], v[102:103]
	v_pk_fma_f32 v[102:103], v[64:65], v[100:101], v[102:103]
	v_exp_f32_e32 v106, v87
	v_pk_mul_f32 v[64:65], v[102:103], v[104:105]
	v_exp_f32_e32 v108, v64
	v_exp_f32_e32 v109, v65
	v_exp_f32_e32 v107, v91
	v_pk_add_f32 v[110:111], v[108:109], 1.0 op_sel_hi:[1,0]
	v_pk_fma_f32 v[110:111], v[110:111], v[106:107], v[110:111]
	v_rcp_f32_e32 v110, v110
	v_rcp_f32_e32 v111, v111
	v_pk_add_f32 v[112:113], v[108:109], -1.0 op_sel_hi:[1,0]
	v_pk_mul_f32 v[112:113], v[112:113], v[110:111]
	v_cvt_pk_f16_f32 v114, v112, v113
	ds_write_b32 v81, v114 offset:0
	s_waitcnt lgkmcnt(0)
	s_setprio 2
	s_barrier
	v_mfma_f32_16x16x32_f16 v[84:87], v[6:9], v[50:53], v[18:21]
	v_mfma_f32_16x16x32_f16 v[88:91], v[10:13], v[50:53], v[38:41]
	ds_read_b128 v[56:59], v75 offset:0
	ds_read_b128 v[60:63], v75 offset:1024
	s_waitcnt vmcnt(3)
	v_mfma_f32_16x16x32_f16 v[84:87], v[2:5], v[46:49], v[84:87]
	v_mfma_f32_16x16x32_f16 v[88:91], v[14:17], v[46:49], v[88:91]
	s_waitcnt lgkmcnt(1)
	v_mfma_f32_16x16x32_f16 v[84:87], v[30:33], v[56:59], v[84:87]
	v_mfma_f32_16x16x32_f16 v[88:91], v[22:25], v[56:59], v[88:91]
	s_waitcnt lgkmcnt(0)
	v_mfma_f32_16x16x32_f16 v[84:87], v[34:37], v[60:63], v[84:87]
	v_mfma_f32_16x16x32_f16 v[88:91], v[26:29], v[60:63], v[88:91]
	s_add_u32 s13, s12, 6
	s_min_u32 s13, s13, 450
	s_cmp_ge_u32 s14, s13
	s_cbranch_scc0 .Lca_slow_18
